# plus v-tile LDS staging loops in chunk A and chunk C issue their four row loads together
# baseline (speedup 1.0000x reference)
.LBB0_645:
	v_ashrrev_i32_e32 v6, 5, v1
	v_mov_b64_e32 v[2:3], s[60:61]
	v_lshlrev_b32_e32 v4, 1, v0
	v_add_u32_e32 v5, s66, v6
	v_and_b32_e32 v136, 0x1f0, v4
	v_mad_i64_i32 v[2:3], s[68:69], v5, s83, v[2:3]
	v_lshl_add_u64 v[20:21], v[2:3], 0, v[136:137]
	v_mul_lo_u32 v6, v6, s72
	v_add3_u32 v6, 0, v6, v136
	s_mov_b64 s[68:69], 0x32000
	v_lshl_add_u64 v[22:23], v[20:21], 0, s[68:69]
	v_lshl_add_u64 v[24:25], v[22:23], 0, s[68:69]
	v_lshl_add_u64 v[26:27], v[24:25], 0, s[68:69]
	global_load_dwordx4 v[2:5], v[20:21], off
	global_load_dwordx4 v[8:11], v[22:23], off
	global_load_dwordx4 v[12:15], v[24:25], off
	global_load_dwordx4 v[16:19], v[26:27], off
	s_waitcnt vmcnt(3)
	ds_write_b128 v6, v[2:5] offset:18432
	s_waitcnt vmcnt(2)
	ds_write_b128 v6, v[8:11] offset:27136
	s_waitcnt vmcnt(1)
	ds_write_b128 v6, v[12:15] offset:35840
	s_waitcnt vmcnt(0)
	ds_write_b128 v6, v[16:19] offset:44544

.LBB0_968:
	v_ashrrev_i32_e32 v6, 5, v1
	v_mov_b64_e32 v[2:3], s[40:41]
	v_lshlrev_b32_e32 v4, 1, v0
	v_add_u32_e32 v5, s74, v6
	v_and_b32_e32 v136, 0x1f0, v4
	v_mad_i64_i32 v[2:3], s[60:61], v5, s83, v[2:3]
	v_lshl_add_u64 v[20:21], v[2:3], 0, v[136:137]
	v_mul_lo_u32 v6, v6, s31
	v_add3_u32 v6, 0, v6, v136
	s_mov_b64 s[60:61], 0x32000
	v_lshl_add_u64 v[22:23], v[20:21], 0, s[60:61]
	v_lshl_add_u64 v[24:25], v[22:23], 0, s[60:61]
	v_lshl_add_u64 v[26:27], v[24:25], 0, s[60:61]
	global_load_dwordx4 v[2:5], v[20:21], off
	global_load_dwordx4 v[8:11], v[22:23], off
	global_load_dwordx4 v[12:15], v[24:25], off
	global_load_dwordx4 v[16:19], v[26:27], off
	s_waitcnt vmcnt(3)
	ds_write_b128 v6, v[2:5] offset:34816
	s_waitcnt vmcnt(2)
	ds_write_b128 v6, v[8:11] offset:43520
	s_waitcnt vmcnt(1)
	ds_write_b128 v6, v[12:15] offset:52224
	s_waitcnt vmcnt(0)
	ds_write_b128 v6, v[16:19] offset:60928
